# pooling window: fma + paired bf16 convert with d16_hi LDS write; attention softmax: packed f32 ops split into scalar pairs
# speedup vs baseline: 1.0834x; 1.0106x over previous
.Lpool_presum_done:
	s_cmp_lg_u32 s1, 0
	s_cbranch_scc1 .Lpool_rows_special
	v_lshlrev_b32_e32 v2, 16, v2
	v_add_f32_e32 v192, v192, v2
	v_lshlrev_b32_e32 v220, 16, v220
	v_fma_f32 v193, v192, s98, -v2
	v_sub_f32_e32 v192, v192, v220
	v_lshlrev_b32_e32 v3, 16, v3
	v_add_f32_e32 v192, v192, v3
	v_lshlrev_b32_e32 v221, 16, v221
	v_fma_f32 v194, v192, s98, -v3
	v_sub_f32_e32 v192, v192, v221
	v_cvt_pk_bf16_f32 v193, v193, v194
	ds_write_b16 v47, v193
	ds_write_b16_d16_hi v47, v193 offset:272
	v_lshlrev_b32_e32 v4, 16, v4
	v_add_f32_e32 v192, v192, v4
	v_lshlrev_b32_e32 v222, 16, v222
	v_fma_f32 v193, v192, s98, -v4
	v_sub_f32_e32 v192, v192, v222
	v_lshlrev_b32_e32 v5, 16, v5
	v_add_f32_e32 v192, v192, v5
	v_lshlrev_b32_e32 v223, 16, v223
	v_fma_f32 v194, v192, s98, -v5
	v_sub_f32_e32 v192, v192, v223
	v_cvt_pk_bf16_f32 v193, v193, v194
	ds_write_b16 v47, v193 offset:544
	ds_write_b16_d16_hi v47, v193 offset:816
	v_lshlrev_b32_e32 v6, 16, v6
	v_add_f32_e32 v192, v192, v6
	v_lshlrev_b32_e32 v224, 16, v224
	v_fma_f32 v193, v192, s98, -v6
	v_sub_f32_e32 v192, v192, v224
	v_lshlrev_b32_e32 v7, 16, v7
	v_add_f32_e32 v192, v192, v7
	v_lshlrev_b32_e32 v225, 16, v225
	v_fma_f32 v194, v192, s98, -v7
	v_sub_f32_e32 v192, v192, v225
	v_cvt_pk_bf16_f32 v193, v193, v194
	ds_write_b16 v47, v193 offset:1088
	ds_write_b16_d16_hi v47, v193 offset:1360
	v_lshlrev_b32_e32 v8, 16, v8
	v_add_f32_e32 v192, v192, v8
	v_lshlrev_b32_e32 v226, 16, v226
	v_fma_f32 v193, v192, s98, -v8
	v_sub_f32_e32 v192, v192, v226
	v_lshlrev_b32_e32 v9, 16, v9
	v_add_f32_e32 v192, v192, v9
	v_lshlrev_b32_e32 v227, 16, v227
	v_fma_f32 v194, v192, s98, -v9
	v_sub_f32_e32 v192, v192, v227
	v_cvt_pk_bf16_f32 v193, v193, v194
	ds_write_b16 v47, v193 offset:1632
	ds_write_b16_d16_hi v47, v193 offset:1904
	v_lshlrev_b32_e32 v10, 16, v10
	v_add_f32_e32 v192, v192, v10
	v_lshlrev_b32_e32 v228, 16, v228
	v_fma_f32 v193, v192, s98, -v10
	v_sub_f32_e32 v192, v192, v228
	v_lshlrev_b32_e32 v11, 16, v11
	v_add_f32_e32 v192, v192, v11
	v_lshlrev_b32_e32 v229, 16, v229
	v_fma_f32 v194, v192, s98, -v11
	v_sub_f32_e32 v192, v192, v229
	v_cvt_pk_bf16_f32 v193, v193, v194
	ds_write_b16 v47, v193 offset:2176
	ds_write_b16_d16_hi v47, v193 offset:2448
	v_lshlrev_b32_e32 v12, 16, v12
	v_add_f32_e32 v192, v192, v12
	v_lshlrev_b32_e32 v230, 16, v230
	v_fma_f32 v193, v192, s98, -v12
	v_sub_f32_e32 v192, v192, v230
	v_lshlrev_b32_e32 v13, 16, v13
	v_add_f32_e32 v192, v192, v13
	v_lshlrev_b32_e32 v231, 16, v231
	v_fma_f32 v194, v192, s98, -v13
	v_sub_f32_e32 v192, v192, v231
	v_cvt_pk_bf16_f32 v193, v193, v194
	ds_write_b16 v47, v193 offset:2720
	ds_write_b16_d16_hi v47, v193 offset:2992
	v_lshlrev_b32_e32 v14, 16, v14
	v_add_f32_e32 v192, v192, v14
	v_lshlrev_b32_e32 v232, 16, v232
	v_fma_f32 v193, v192, s98, -v14
	v_sub_f32_e32 v192, v192, v232
	v_lshlrev_b32_e32 v15, 16, v15
	v_add_f32_e32 v192, v192, v15
	v_lshlrev_b32_e32 v233, 16, v233
	v_fma_f32 v194, v192, s98, -v15
	v_sub_f32_e32 v192, v192, v233
	v_cvt_pk_bf16_f32 v193, v193, v194
	ds_write_b16 v47, v193 offset:3264
	ds_write_b16_d16_hi v47, v193 offset:3536
	v_lshlrev_b32_e32 v16, 16, v16
	v_add_f32_e32 v192, v192, v16
	v_lshlrev_b32_e32 v234, 16, v234
	v_fma_f32 v193, v192, s98, -v16
	v_sub_f32_e32 v192, v192, v234
	v_lshlrev_b32_e32 v17, 16, v17
	v_add_f32_e32 v192, v192, v17
	v_lshlrev_b32_e32 v235, 16, v235
	v_fma_f32 v194, v192, s98, -v17
	v_sub_f32_e32 v192, v192, v235
	v_cvt_pk_bf16_f32 v193, v193, v194
	ds_write_b16 v47, v193 offset:3808
	ds_write_b16_d16_hi v47, v193 offset:4080
	s_branch .Lpool_rows_16
.Lpool_rows_special:
	s_min_u32 s0, 1, s99
	v_cvt_f32_u32_e32 v194, s0
	v_lshlrev_b32_e32 v2, 16, v2
	v_rcp_f32_e32 v1, v194
	v_add_f32_e32 v192, v192, v2
	v_lshlrev_b32_e32 v220, 16, v220
	v_mul_f32_e32 v193, v192, v1
	v_fma_f32 v50, -v194, v193, v192
	v_fmac_f32_e32 v193, v50, v1
	v_sub_f32_e32 v193, v193, v2
	v_sub_f32_e32 v192, v192, v220
	v_cvt_pk_bf16_f32 v193, v193, v195
	ds_write_b16 v47, v193
	s_min_u32 s0, 2, s99
	v_cvt_f32_u32_e32 v194, s0
	v_lshlrev_b32_e32 v3, 16, v3
	v_rcp_f32_e32 v1, v194
	v_add_f32_e32 v192, v192, v3
	v_lshlrev_b32_e32 v221, 16, v221
	v_mul_f32_e32 v193, v192, v1
	v_fma_f32 v50, -v194, v193, v192
	v_fmac_f32_e32 v193, v50, v1
	v_sub_f32_e32 v193, v193, v3
	v_sub_f32_e32 v192, v192, v221
	v_cvt_pk_bf16_f32 v193, v193, v195
	ds_write_b16 v47, v193 offset:272
	s_min_u32 s0, 3, s99
	v_cvt_f32_u32_e32 v194, s0
	v_lshlrev_b32_e32 v4, 16, v4
	v_rcp_f32_e32 v1, v194
	v_add_f32_e32 v192, v192, v4
	v_lshlrev_b32_e32 v222, 16, v222
	v_mul_f32_e32 v193, v192, v1
	v_fma_f32 v50, -v194, v193, v192
	v_fmac_f32_e32 v193, v50, v1
	v_sub_f32_e32 v193, v193, v4
	v_sub_f32_e32 v192, v192, v222
	v_cvt_pk_bf16_f32 v193, v193, v195
	ds_write_b16 v47, v193 offset:544
	s_min_u32 s0, 4, s99
	v_cvt_f32_u32_e32 v194, s0
	v_lshlrev_b32_e32 v5, 16, v5
	v_rcp_f32_e32 v1, v194
	v_add_f32_e32 v192, v192, v5
	v_lshlrev_b32_e32 v223, 16, v223
	v_mul_f32_e32 v193, v192, v1
	v_fma_f32 v50, -v194, v193, v192
	v_fmac_f32_e32 v193, v50, v1
	v_sub_f32_e32 v193, v193, v5
	v_sub_f32_e32 v192, v192, v223
	v_cvt_pk_bf16_f32 v193, v193, v195
	ds_write_b16 v47, v193 offset:816
	s_min_u32 s0, 5, s99
	v_cvt_f32_u32_e32 v194, s0
	v_lshlrev_b32_e32 v6, 16, v6
	v_rcp_f32_e32 v1, v194
	v_add_f32_e32 v192, v192, v6
	v_lshlrev_b32_e32 v224, 16, v224
	v_mul_f32_e32 v193, v192, v1
	v_fma_f32 v50, -v194, v193, v192
	v_fmac_f32_e32 v193, v50, v1
	v_sub_f32_e32 v193, v193, v6
	v_sub_f32_e32 v192, v192, v224
	v_cvt_pk_bf16_f32 v193, v193, v195
	ds_write_b16 v47, v193 offset:1088
	s_min_u32 s0, 6, s99
	v_cvt_f32_u32_e32 v194, s0
	v_lshlrev_b32_e32 v7, 16, v7
	v_rcp_f32_e32 v1, v194
	v_add_f32_e32 v192, v192, v7
	v_lshlrev_b32_e32 v225, 16, v225
	v_mul_f32_e32 v193, v192, v1
	v_fma_f32 v50, -v194, v193, v192
	v_fmac_f32_e32 v193, v50, v1
	v_sub_f32_e32 v193, v193, v7
	v_sub_f32_e32 v192, v192, v225
	v_cvt_pk_bf16_f32 v193, v193, v195
	ds_write_b16 v47, v193 offset:1360
	s_min_u32 s0, 7, s99
	v_cvt_f32_u32_e32 v194, s0
	v_lshlrev_b32_e32 v8, 16, v8
	v_rcp_f32_e32 v1, v194
	v_add_f32_e32 v192, v192, v8
	v_lshlrev_b32_e32 v226, 16, v226
	v_mul_f32_e32 v193, v192, v1
	v_fma_f32 v50, -v194, v193, v192
	v_fmac_f32_e32 v193, v50, v1
	v_sub_f32_e32 v193, v193, v8
	v_sub_f32_e32 v192, v192, v226
	v_cvt_pk_bf16_f32 v193, v193, v195
	ds_write_b16 v47, v193 offset:1632
	s_min_u32 s0, 8, s99
	v_cvt_f32_u32_e32 v194, s0
	v_lshlrev_b32_e32 v9, 16, v9
	v_rcp_f32_e32 v1, v194
	v_add_f32_e32 v192, v192, v9
	v_lshlrev_b32_e32 v227, 16, v227
	v_mul_f32_e32 v193, v192, v1
	v_fma_f32 v50, -v194, v193, v192
	v_fmac_f32_e32 v193, v50, v1
	v_sub_f32_e32 v193, v193, v9
	v_sub_f32_e32 v192, v192, v227
	v_cvt_pk_bf16_f32 v193, v193, v195
	ds_write_b16 v47, v193 offset:1904
	s_min_u32 s0, 9, s99
	v_cvt_f32_u32_e32 v194, s0
	v_lshlrev_b32_e32 v10, 16, v10
	v_rcp_f32_e32 v1, v194
	v_add_f32_e32 v192, v192, v10
	v_lshlrev_b32_e32 v228, 16, v228
	v_mul_f32_e32 v193, v192, v1
	v_fma_f32 v50, -v194, v193, v192
	v_fmac_f32_e32 v193, v50, v1
	v_sub_f32_e32 v193, v193, v10
	v_sub_f32_e32 v192, v192, v228
	v_cvt_pk_bf16_f32 v193, v193, v195
	ds_write_b16 v47, v193 offset:2176
	s_min_u32 s0, 10, s99
	v_cvt_f32_u32_e32 v194, s0
	v_lshlrev_b32_e32 v11, 16, v11
	v_rcp_f32_e32 v1, v194
	v_add_f32_e32 v192, v192, v11
	v_lshlrev_b32_e32 v229, 16, v229
	v_mul_f32_e32 v193, v192, v1
	v_fma_f32 v50, -v194, v193, v192
	v_fmac_f32_e32 v193, v50, v1
	v_sub_f32_e32 v193, v193, v11
	v_sub_f32_e32 v192, v192, v229
	v_cvt_pk_bf16_f32 v193, v193, v195
	ds_write_b16 v47, v193 offset:2448
	s_min_u32 s0, 11, s99
	v_cvt_f32_u32_e32 v194, s0
	v_lshlrev_b32_e32 v12, 16, v12
	v_rcp_f32_e32 v1, v194
	v_add_f32_e32 v192, v192, v12
	v_lshlrev_b32_e32 v230, 16, v230
	v_mul_f32_e32 v193, v192, v1
	v_fma_f32 v50, -v194, v193, v192
	v_fmac_f32_e32 v193, v50, v1
	v_sub_f32_e32 v193, v193, v12
	v_sub_f32_e32 v192, v192, v230
	v_cvt_pk_bf16_f32 v193, v193, v195
	ds_write_b16 v47, v193 offset:2720
	s_min_u32 s0, 12, s99
	v_cvt_f32_u32_e32 v194, s0
	v_lshlrev_b32_e32 v13, 16, v13
	v_rcp_f32_e32 v1, v194
	v_add_f32_e32 v192, v192, v13
	v_lshlrev_b32_e32 v231, 16, v231
	v_mul_f32_e32 v193, v192, v1
	v_fma_f32 v50, -v194, v193, v192
	v_fmac_f32_e32 v193, v50, v1
	v_sub_f32_e32 v193, v193, v13
	v_sub_f32_e32 v192, v192, v231
	v_cvt_pk_bf16_f32 v193, v193, v195
	ds_write_b16 v47, v193 offset:2992
	s_min_u32 s0, 13, s99
	v_cvt_f32_u32_e32 v194, s0
	v_lshlrev_b32_e32 v14, 16, v14
	v_rcp_f32_e32 v1, v194
	v_add_f32_e32 v192, v192, v14
	v_lshlrev_b32_e32 v232, 16, v232
	v_mul_f32_e32 v193, v192, v1
	v_fma_f32 v50, -v194, v193, v192
	v_fmac_f32_e32 v193, v50, v1
	v_sub_f32_e32 v193, v193, v14
	v_sub_f32_e32 v192, v192, v232
	v_cvt_pk_bf16_f32 v193, v193, v195
	ds_write_b16 v47, v193 offset:3264
	s_min_u32 s0, 14, s99
	v_cvt_f32_u32_e32 v194, s0
	v_lshlrev_b32_e32 v15, 16, v15
	v_rcp_f32_e32 v1, v194
	v_add_f32_e32 v192, v192, v15
	v_lshlrev_b32_e32 v233, 16, v233
	v_mul_f32_e32 v193, v192, v1
	v_fma_f32 v50, -v194, v193, v192
	v_fmac_f32_e32 v193, v50, v1
	v_sub_f32_e32 v193, v193, v15
	v_sub_f32_e32 v192, v192, v233
	v_cvt_pk_bf16_f32 v193, v193, v195
	ds_write_b16 v47, v193 offset:3536
	s_min_u32 s0, 15, s99
	v_cvt_f32_u32_e32 v194, s0
	v_lshlrev_b32_e32 v16, 16, v16
	v_rcp_f32_e32 v1, v194
	v_add_f32_e32 v192, v192, v16
	v_lshlrev_b32_e32 v234, 16, v234
	v_mul_f32_e32 v193, v192, v1
	v_fma_f32 v50, -v194, v193, v192
	v_fmac_f32_e32 v193, v50, v1
	v_sub_f32_e32 v193, v193, v16
	v_sub_f32_e32 v192, v192, v234
	v_cvt_pk_bf16_f32 v193, v193, v195
	ds_write_b16 v47, v193 offset:3808
	v_lshlrev_b32_e32 v17, 16, v17
	v_add_f32_e32 v192, v192, v17
	v_lshlrev_b32_e32 v235, 16, v235
	v_fma_f32 v193, v192, s98, -v17
	v_sub_f32_e32 v192, v192, v235
	v_cvt_pk_bf16_f32 v193, v193, v195
	ds_write_b16 v47, v193 offset:4080
.Lpool_rows_16:
	s_waitcnt lgkmcnt(0)
	v_lshlrev_b32_e32 v18, 16, v18
	v_add_f32_e32 v192, v192, v18
	v_lshlrev_b32_e32 v236, 16, v236
	v_fma_f32 v193, v192, s98, -v18
	v_sub_f32_e32 v192, v192, v236
	v_lshlrev_b32_e32 v19, 16, v19
	v_add_f32_e32 v192, v192, v19
	v_lshlrev_b32_e32 v237, 16, v237
	v_fma_f32 v194, v192, s98, -v19
	v_sub_f32_e32 v192, v192, v237
	v_cvt_pk_bf16_f32 v193, v193, v194
	ds_write_b16 v47, v193 offset:4352
	ds_write_b16_d16_hi v47, v193 offset:4624
	v_lshlrev_b32_e32 v20, 16, v20
	v_add_f32_e32 v192, v192, v20
	v_lshlrev_b32_e32 v238, 16, v238
	v_fma_f32 v193, v192, s98, -v20
	v_sub_f32_e32 v192, v192, v238
	v_lshlrev_b32_e32 v21, 16, v21
	v_add_f32_e32 v192, v192, v21
	v_lshlrev_b32_e32 v239, 16, v239
	v_fma_f32 v194, v192, s98, -v21
	v_sub_f32_e32 v192, v192, v239
	v_cvt_pk_bf16_f32 v193, v193, v194
	ds_write_b16 v47, v193 offset:4896
	ds_write_b16_d16_hi v47, v193 offset:5168
	v_lshlrev_b32_e32 v22, 16, v22
	v_add_f32_e32 v192, v192, v22
	v_lshlrev_b32_e32 v240, 16, v240
	v_fma_f32 v193, v192, s98, -v22
	v_sub_f32_e32 v192, v192, v240
	v_lshlrev_b32_e32 v23, 16, v23
	v_add_f32_e32 v192, v192, v23
	v_lshlrev_b32_e32 v241, 16, v241
	v_fma_f32 v194, v192, s98, -v23
	v_sub_f32_e32 v192, v192, v241
	v_cvt_pk_bf16_f32 v193, v193, v194
	ds_write_b16 v47, v193 offset:5440
	ds_write_b16_d16_hi v47, v193 offset:5712
	v_lshlrev_b32_e32 v24, 16, v24
	v_add_f32_e32 v192, v192, v24
	v_lshlrev_b32_e32 v242, 16, v242
	v_fma_f32 v193, v192, s98, -v24
	v_sub_f32_e32 v192, v192, v242
	v_lshlrev_b32_e32 v25, 16, v25
	v_add_f32_e32 v192, v192, v25
	v_lshlrev_b32_e32 v243, 16, v243
	v_fma_f32 v194, v192, s98, -v25
	v_sub_f32_e32 v192, v192, v243
	v_cvt_pk_bf16_f32 v193, v193, v194
	ds_write_b16 v47, v193 offset:5984
	ds_write_b16_d16_hi v47, v193 offset:6256
	v_lshlrev_b32_e32 v26, 16, v26
	v_add_f32_e32 v192, v192, v26
	v_lshlrev_b32_e32 v244, 16, v244
	v_fma_f32 v193, v192, s98, -v26
	v_sub_f32_e32 v192, v192, v244
	v_lshlrev_b32_e32 v27, 16, v27
	v_add_f32_e32 v192, v192, v27
	v_lshlrev_b32_e32 v245, 16, v245
	v_fma_f32 v194, v192, s98, -v27
	v_sub_f32_e32 v192, v192, v245
	v_cvt_pk_bf16_f32 v193, v193, v194
	ds_write_b16 v47, v193 offset:6528
	ds_write_b16_d16_hi v47, v193 offset:6800
	v_lshlrev_b32_e32 v28, 16, v28
	v_add_f32_e32 v192, v192, v28
	v_lshlrev_b32_e32 v246, 16, v246
	v_fma_f32 v193, v192, s98, -v28
	v_sub_f32_e32 v192, v192, v246
	v_lshlrev_b32_e32 v29, 16, v29
	v_add_f32_e32 v192, v192, v29
	v_lshlrev_b32_e32 v247, 16, v247
	v_fma_f32 v194, v192, s98, -v29
	v_sub_f32_e32 v192, v192, v247
	v_cvt_pk_bf16_f32 v193, v193, v194
	ds_write_b16 v47, v193 offset:7072
	ds_write_b16_d16_hi v47, v193 offset:7344
	v_lshlrev_b32_e32 v30, 16, v30
	v_add_f32_e32 v192, v192, v30
	v_lshlrev_b32_e32 v248, 16, v248
	v_fma_f32 v193, v192, s98, -v30
	v_sub_f32_e32 v192, v192, v248
	v_lshlrev_b32_e32 v31, 16, v31
	v_add_f32_e32 v192, v192, v31
	v_lshlrev_b32_e32 v249, 16, v249
	v_fma_f32 v194, v192, s98, -v31
	v_sub_f32_e32 v192, v192, v249
	v_cvt_pk_bf16_f32 v193, v193, v194
	ds_write_b16 v47, v193 offset:7616
	ds_write_b16_d16_hi v47, v193 offset:7888
	v_lshlrev_b32_e32 v32, 16, v32
	v_add_f32_e32 v192, v192, v32
	v_lshlrev_b32_e32 v250, 16, v250
	v_fma_f32 v193, v192, s98, -v32
	v_sub_f32_e32 v192, v192, v250
	v_lshlrev_b32_e32 v33, 16, v33
	v_add_f32_e32 v192, v192, v33
	v_lshlrev_b32_e32 v251, 16, v251
	v_fma_f32 v194, v192, s98, -v33
	v_sub_f32_e32 v192, v192, v251
	v_cvt_pk_bf16_f32 v193, v193, v194
	ds_write_b16 v47, v193 offset:8160
	ds_write_b16_d16_hi v47, v193 offset:8432
	s_waitcnt lgkmcnt(0)
	s_barrier
	ds_read_b128 v[220:223], v51
	ds_read_b128 v[224:227], v51 offset:32
	ds_read_b128 v[228:231], v51 offset:64
	ds_read_b128 v[232:235], v51 offset:96
	ds_read_b128 v[236:239], v51 offset:128
	ds_read_b128 v[240:243], v51 offset:160
	ds_read_b128 v[244:247], v51 offset:192
	ds_read_b128 v[248:251], v51 offset:224
	s_lshl_b32 s22, s17, 10
	s_lshl_b32 s23, s16, 7
	s_add_i32 s22, s22, s23
	s_add_u32 s18, s40, s22
	s_addc_u32 s19, s41, 0
	s_waitcnt lgkmcnt(7)
	v_mfma_f32_32x32x16_bf16 v[2:17], v[128:131], v[220:223], 0
	v_mfma_f32_32x32x16_bf16 v[18:33], v[160:163], v[220:223], 0
	s_waitcnt lgkmcnt(6)
	v_mfma_f32_32x32x16_bf16 v[2:17], v[132:135], v[224:227], v[2:17]
	v_mfma_f32_32x32x16_bf16 v[18:33], v[164:167], v[224:227], v[18:33]
	s_waitcnt lgkmcnt(5)
	v_mfma_f32_32x32x16_bf16 v[2:17], v[136:139], v[228:231], v[2:17]
	v_mfma_f32_32x32x16_bf16 v[18:33], v[168:171], v[228:231], v[18:33]
	s_waitcnt lgkmcnt(4)
	v_mfma_f32_32x32x16_bf16 v[2:17], v[140:143], v[232:235], v[2:17]
	v_mfma_f32_32x32x16_bf16 v[18:33], v[172:175], v[232:235], v[18:33]
	s_waitcnt lgkmcnt(3)
	v_mfma_f32_32x32x16_bf16 v[2:17], v[144:147], v[236:239], v[2:17]
	v_mfma_f32_32x32x16_bf16 v[18:33], v[176:179], v[236:239], v[18:33]
	s_waitcnt lgkmcnt(2)
	v_mfma_f32_32x32x16_bf16 v[2:17], v[148:151], v[240:243], v[2:17]
	v_mfma_f32_32x32x16_bf16 v[18:33], v[180:183], v[240:243], v[18:33]
	s_waitcnt lgkmcnt(1)
	v_mfma_f32_32x32x16_bf16 v[2:17], v[152:155], v[244:247], v[2:17]
	v_mfma_f32_32x32x16_bf16 v[18:33], v[184:187], v[244:247], v[18:33]
	s_waitcnt lgkmcnt(0)
	v_mfma_f32_32x32x16_bf16 v[2:17], v[156:159], v[248:251], v[2:17]
	v_mfma_f32_32x32x16_bf16 v[18:33], v[188:191], v[248:251], v[18:33]
	s_add_i32 s14, s14, s72
	s_add_i32 s21, s21, 1
	s_nop 7
	s_nop 3
	v_mul_f32_e32 v2, v2, v96
	v_mul_f32_e32 v3, v3, v97
	v_mul_f32_e32 v4, v4, v98
	v_mul_f32_e32 v5, v5, v99
	v_med3_f32 v2, v2, s100, v55
	v_med3_f32 v3, v3, s100, v55
	v_med3_f32 v4, v4, s100, v55
	v_med3_f32 v5, v5, s100, v55
	v_cvt_pk_fp8_f32 v198, v2, v3
	s_nop 0
	v_cvt_pk_fp8_f32 v198, v4, v5 op_sel:[0,0,1]
	v_mul_f32_e32 v6, v6, v100
	v_mul_f32_e32 v7, v7, v101
	v_mul_f32_e32 v8, v8, v102
	v_mul_f32_e32 v9, v9, v103
	v_med3_f32 v6, v6, s100, v55
	v_med3_f32 v7, v7, s100, v55
	v_med3_f32 v8, v8, s100, v55
	v_med3_f32 v9, v9, s100, v55
	v_cvt_pk_fp8_f32 v199, v6, v7
	s_nop 0
	v_cvt_pk_fp8_f32 v199, v8, v9 op_sel:[0,0,1]
	v_mul_f32_e32 v10, v10, v104
	v_mul_f32_e32 v11, v11, v105
	v_mul_f32_e32 v12, v12, v106
	v_mul_f32_e32 v13, v13, v107
	v_med3_f32 v10, v10, s100, v55
	v_med3_f32 v11, v11, s100, v55
	v_med3_f32 v12, v12, s100, v55
	v_med3_f32 v13, v13, s100, v55
	v_cvt_pk_fp8_f32 v200, v10, v11
	s_nop 0
	v_cvt_pk_fp8_f32 v200, v12, v13 op_sel:[0,0,1]
	v_mul_f32_e32 v14, v14, v108
	v_mul_f32_e32 v15, v15, v109
	v_mul_f32_e32 v16, v16, v110
	v_mul_f32_e32 v17, v17, v111
	v_med3_f32 v14, v14, s100, v55
	v_med3_f32 v15, v15, s100, v55
	v_med3_f32 v16, v16, s100, v55
	v_med3_f32 v17, v17, s100, v55
	v_cvt_pk_fp8_f32 v201, v14, v15
	s_nop 0
	v_cvt_pk_fp8_f32 v201, v16, v17 op_sel:[0,0,1]
	v_mul_f32_e32 v18, v18, v112
	v_mul_f32_e32 v19, v19, v113
	v_mul_f32_e32 v20, v20, v114
	v_mul_f32_e32 v21, v21, v115
	v_med3_f32 v18, v18, s100, v55
	v_med3_f32 v19, v19, s100, v55
	v_med3_f32 v20, v20, s100, v55
	v_med3_f32 v21, v21, s100, v55
	v_cvt_pk_fp8_f32 v202, v18, v19
	s_nop 0
	v_cvt_pk_fp8_f32 v202, v20, v21 op_sel:[0,0,1]
	v_mul_f32_e32 v22, v22, v116
	v_mul_f32_e32 v23, v23, v117
	v_mul_f32_e32 v24, v24, v118
	v_mul_f32_e32 v25, v25, v119
	v_med3_f32 v22, v22, s100, v55
	v_med3_f32 v23, v23, s100, v55
	v_med3_f32 v24, v24, s100, v55
	v_med3_f32 v25, v25, s100, v55
	v_cvt_pk_fp8_f32 v203, v22, v23
	s_nop 0
	v_cvt_pk_fp8_f32 v203, v24, v25 op_sel:[0,0,1]
	v_mul_f32_e32 v26, v26, v120
	v_mul_f32_e32 v27, v27, v121
	v_mul_f32_e32 v28, v28, v122
	v_mul_f32_e32 v29, v29, v123
	v_med3_f32 v26, v26, s100, v55
	v_med3_f32 v27, v27, s100, v55
	v_med3_f32 v28, v28, s100, v55
	v_med3_f32 v29, v29, s100, v55
	v_cvt_pk_fp8_f32 v204, v26, v27
	s_nop 0
	v_cvt_pk_fp8_f32 v204, v28, v29 op_sel:[0,0,1]
	v_mul_f32_e32 v30, v30, v124
	v_mul_f32_e32 v31, v31, v125
	v_mul_f32_e32 v32, v32, v126
	v_mul_f32_e32 v33, v33, v127
	v_med3_f32 v30, v30, s100, v55
	v_med3_f32 v31, v31, s100, v55
	v_med3_f32 v32, v32, s100, v55
	v_med3_f32 v33, v33, s100, v55
	v_cvt_pk_fp8_f32 v205, v30, v31
	s_nop 0
	v_cvt_pk_fp8_f32 v205, v32, v33 op_sel:[0,0,1]
	s_nop 1
	v_permlane32_swap_b32_e32 v198, v199
	v_permlane32_swap_b32_e32 v200, v201
	v_permlane32_swap_b32_e32 v202, v203
	v_permlane32_swap_b32_e32 v204, v205
	s_nop 0
	global_store_dwordx2 v54, v[198:199], s[18:19]
	global_store_dwordx2 v54, v[200:201], s[18:19] offset:16
	global_store_dwordx2 v54, v[202:203], s[18:19] offset:32
	global_store_dwordx2 v54, v[204:205], s[18:19] offset:48
	s_cmpk_lt_u32 s14, 0x800
	s_cbranch_scc1 .Lpool_unit

.LBB0_372:
	s_cmpk_lg_i32 s81, 0xfc00
	s_cselect_b64 s[36:37], -1, 0
	s_cmpk_eq_i32 s81, 0xfc00
	s_cbranch_scc1 .LBB0_384
	s_add_i32 s6, s82, -2
	s_cmp_gt_i32 s6, s62
	s_cbranch_scc1 .LBB0_384
	s_add_i32 s6, s67, s80
	s_cmpk_lt_i32 s6, 0xffa6
	s_cbranch_scc1 .LBB0_376
	v_add_u32_e32 v2, s81, v218
	v_add_u32_e32 v4, 0x205e0, v2
	v_add_u32_e32 v6, 0x20660, v2
	ds_read2_b32 v[4:5], v4 offset1:1
	ds_read2_b32 v[6:7], v6 offset1:1
	v_add_u32_e32 v8, 0x205e8, v2
	v_add_u32_e32 v10, 0x20668, v2
	v_add_u32_e32 v12, 0x20600, v2
	v_add_u32_e32 v14, 0x20680, v2
	v_add_u32_e32 v16, 0x20608, v2
	v_add_u32_e32 v178, 0x20688, v2
	v_add_u32_e32 v180, 0x20620, v2
	v_add_u32_e32 v182, 0x206a0, v2
	v_add_u32_e32 v184, 0x20628, v2
	v_add_u32_e32 v186, 0x206a8, v2
	v_add_u32_e32 v188, 0x20640, v2
	v_add_u32_e32 v190, 0x206c0, v2
	v_add_u32_e32 v192, 0x20648, v2
	v_add_u32_e32 v2, 0x206c8, v2
	ds_read2_b32 v[8:9], v8 offset1:1
	ds_read2_b32 v[10:11], v10 offset1:1
	ds_read2_b32 v[12:13], v12 offset1:1
	ds_read2_b32 v[14:15], v14 offset1:1
	ds_read2_b32 v[16:17], v16 offset1:1
	ds_read2_b32 v[178:179], v178 offset1:1
	ds_read2_b32 v[180:181], v180 offset1:1
	ds_read2_b32 v[182:183], v182 offset1:1
	ds_read2_b32 v[184:185], v184 offset1:1
	ds_read2_b32 v[186:187], v186 offset1:1
	ds_read2_b32 v[188:189], v188 offset1:1
	ds_read2_b32 v[190:191], v190 offset1:1
	ds_read2_b32 v[192:193], v192 offset1:1
	s_waitcnt lgkmcnt(14)
	v_add_f32_e32 v162, v162, v4
	v_add_f32_e32 v163, v163, v5
	ds_read2_b32 v[4:5], v2 offset1:1
	s_waitcnt lgkmcnt(3)
	v_add_f32_e32 v174, v174, v188
	v_add_f32_e32 v175, v175, v189
	v_add_f32_e32 v172, v172, v184
	v_add_f32_e32 v173, v173, v185
	s_waitcnt lgkmcnt(1)
	v_add_f32_e32 v176, v176, v192
	v_add_f32_e32 v177, v177, v193
	v_add_f32_e32 v170, v170, v180
	v_add_f32_e32 v171, v171, v181
	v_add_f32_e32 v168, v168, v16
	v_add_f32_e32 v169, v169, v17
	v_add_f32_e32 v166, v166, v12
	v_add_f32_e32 v167, v167, v13
	v_add_f32_e32 v164, v164, v8
	v_add_f32_e32 v165, v165, v9
	s_waitcnt lgkmcnt(0)
	v_add_f32_e32 v160, v160, v4
	v_add_f32_e32 v161, v161, v5
	v_add_f32_e32 v158, v158, v190
	v_add_f32_e32 v159, v159, v191
	v_add_f32_e32 v156, v156, v186
	v_add_f32_e32 v157, v157, v187
	v_add_f32_e32 v154, v154, v182
	v_add_f32_e32 v155, v155, v183
	v_add_f32_e32 v152, v152, v178
	v_add_f32_e32 v153, v153, v179
	v_add_f32_e32 v150, v150, v14
	v_add_f32_e32 v151, v151, v15
	v_add_f32_e32 v148, v148, v10
	v_add_f32_e32 v149, v149, v11
	v_add_f32_e32 v146, v146, v6
	v_add_f32_e32 v147, v147, v7

.LBB0_379:
	s_and_b64 vcc, exec, s[38:39]
	s_cbranch_vccz .LBB0_383
	s_andn2_b64 vcc, exec, s[10:11]
	s_cbranch_vccnz .LBB0_382
	v_exp_f32_e64 v4, -v2
	s_nop 0
	v_mul_f32_e32 v144, v144, v4
	v_mul_f32_e32 v145, v145, v4
	v_mul_f32_e32 v142, v142, v4
	v_mul_f32_e32 v143, v143, v4
	v_mul_f32_e32 v140, v140, v4
	v_mul_f32_e32 v141, v141, v4
	v_mul_f32_e32 v138, v138, v4
	v_mul_f32_e32 v139, v139, v4
	v_mul_f32_e32 v136, v136, v4
	v_mul_f32_e32 v137, v137, v4
	v_mul_f32_e32 v134, v134, v4
	v_mul_f32_e32 v135, v135, v4
	v_mul_f32_e32 v132, v132, v4
	v_mul_f32_e32 v133, v133, v4
	v_mul_f32_e32 v130, v130, v4
	v_mul_f32_e32 v131, v131, v4
	v_mul_f32_e32 v112, v112, v4
	v_mul_f32_e32 v113, v113, v4
	v_mul_f32_e32 v110, v110, v4
	v_mul_f32_e32 v111, v111, v4
	v_mul_f32_e32 v108, v108, v4
	v_mul_f32_e32 v109, v109, v4
	v_mul_f32_e32 v106, v106, v4
	v_mul_f32_e32 v107, v107, v4
	v_mul_f32_e32 v104, v104, v4
	v_mul_f32_e32 v105, v105, v4
	v_mul_f32_e32 v102, v102, v4
	v_mul_f32_e32 v103, v103, v4
	v_mul_f32_e32 v100, v100, v4
	v_mul_f32_e32 v101, v101, v4
	v_mul_f32_e32 v98, v98, v4
	v_mul_f32_e32 v99, v99, v4
	v_mul_f32_e32 v80, v80, v4
	v_mul_f32_e32 v81, v81, v4
	v_mul_f32_e32 v78, v78, v4
	v_mul_f32_e32 v79, v79, v4
	v_mul_f32_e32 v76, v76, v4
	v_mul_f32_e32 v77, v77, v4
	v_mul_f32_e32 v74, v74, v4
	v_mul_f32_e32 v75, v75, v4
	v_mul_f32_e32 v72, v72, v4
	v_mul_f32_e32 v73, v73, v4
	v_mul_f32_e32 v70, v70, v4
	v_mul_f32_e32 v71, v71, v4
	v_mul_f32_e32 v68, v68, v4
	v_mul_f32_e32 v69, v69, v4
	v_mul_f32_e32 v66, v66, v4
	v_mul_f32_e32 v67, v67, v4
	v_mul_f32_e32 v48, v48, v4
	v_mul_f32_e32 v49, v49, v4
	v_mul_f32_e32 v46, v46, v4
	v_mul_f32_e32 v47, v47, v4
	v_mul_f32_e32 v44, v44, v4
	v_mul_f32_e32 v45, v45, v4
	v_mul_f32_e32 v42, v42, v4
	v_mul_f32_e32 v43, v43, v4
	v_mul_f32_e32 v40, v40, v4
	v_mul_f32_e32 v41, v41, v4
	v_mul_f32_e32 v38, v38, v4
	v_mul_f32_e32 v39, v39, v4
	v_mul_f32_e32 v36, v36, v4
	v_mul_f32_e32 v37, v37, v4
	v_mul_f32_e32 v34, v34, v4
	v_mul_f32_e32 v35, v35, v4
	v_mul_f32_e32 v215, v215, v4
.LBB0_382:
	v_sub_f32_e32 v162, v162, v2
	v_sub_f32_e32 v163, v163, v2
	v_sub_f32_e32 v146, v146, v2
	v_sub_f32_e32 v147, v147, v2
	v_sub_f32_e32 v164, v164, v2
	v_sub_f32_e32 v165, v165, v2
	v_sub_f32_e32 v148, v148, v2
	v_sub_f32_e32 v149, v149, v2
	v_sub_f32_e32 v166, v166, v2
	v_sub_f32_e32 v167, v167, v2
	v_sub_f32_e32 v150, v150, v2
	v_sub_f32_e32 v151, v151, v2
	v_sub_f32_e32 v168, v168, v2
	v_sub_f32_e32 v169, v169, v2
	v_sub_f32_e32 v152, v152, v2
	v_sub_f32_e32 v153, v153, v2
	v_sub_f32_e32 v170, v170, v2
	v_sub_f32_e32 v171, v171, v2
	v_sub_f32_e32 v154, v154, v2
	v_sub_f32_e32 v155, v155, v2
	v_sub_f32_e32 v172, v172, v2
	v_sub_f32_e32 v173, v173, v2
	v_sub_f32_e32 v156, v156, v2
	v_sub_f32_e32 v157, v157, v2
	v_sub_f32_e32 v174, v174, v2
	v_sub_f32_e32 v175, v175, v2
	v_sub_f32_e32 v158, v158, v2
	v_sub_f32_e32 v159, v159, v2
	v_sub_f32_e32 v176, v176, v2
	v_sub_f32_e32 v177, v177, v2
	v_sub_f32_e32 v160, v160, v2
	v_sub_f32_e32 v161, v161, v2
	v_add_f32_e32 v220, v220, v2
.LBB0_383:
	v_exp_f32_e32 v162, v162
	v_exp_f32_e32 v146, v146
	v_exp_f32_e32 v163, v163
	v_exp_f32_e32 v147, v147
	v_exp_f32_e32 v164, v164
	v_exp_f32_e32 v148, v148
	v_exp_f32_e32 v165, v165
	v_exp_f32_e32 v149, v149
	v_exp_f32_e32 v166, v166
	v_exp_f32_e32 v150, v150
	v_exp_f32_e32 v167, v167
	v_exp_f32_e32 v151, v151
	v_exp_f32_e32 v168, v168
	v_exp_f32_e32 v152, v152
	v_exp_f32_e32 v169, v169
	v_exp_f32_e32 v153, v153
	v_exp_f32_e32 v170, v170
	v_exp_f32_e32 v154, v154
	v_exp_f32_e32 v171, v171
	v_exp_f32_e32 v155, v155
	v_exp_f32_e32 v172, v172
	v_exp_f32_e32 v156, v156
	v_exp_f32_e32 v173, v173
	v_exp_f32_e32 v157, v157
	v_exp_f32_e32 v174, v174
	v_exp_f32_e32 v158, v158
	v_exp_f32_e32 v175, v175
	v_exp_f32_e32 v176, v176
	v_exp_f32_e32 v160, v160
	v_exp_f32_e32 v177, v177
	v_exp_f32_e32 v161, v161
	v_exp_f32_e32 v159, v159
	v_add_f32_e32 v4, v156, v172
	v_add_f32_e32 v5, v157, v173
	v_add_f32_e32 v6, v148, v164
	v_add_f32_e32 v7, v149, v165
	v_add_f32_e32 v8, v160, v176
	v_add_f32_e32 v9, v161, v177
	v_add_f32_e32 v10, v152, v168
	v_add_f32_e32 v11, v153, v169
	v_add_f32_e32 v12, v154, v170
	v_add_f32_e32 v13, v155, v171
	v_add_f32_e32 v14, v146, v162
	v_add_f32_e32 v15, v147, v163
	v_add_f32_e32 v16, v158, v174
	v_add_f32_e32 v17, v159, v175
	v_add_f32_e32 v178, v150, v166
	v_add_f32_e32 v179, v151, v167
	v_add_f32_e32 v12, v14, v12
	v_add_f32_e32 v13, v15, v13
	v_add_f32_e32 v16, v178, v16
	v_add_f32_e32 v17, v179, v17
	v_add_f32_e32 v8, v10, v8
	v_add_f32_e32 v9, v11, v9
	v_add_f32_e32 v4, v6, v4
	v_add_f32_e32 v5, v7, v5
	v_add_f32_e32 v6, v12, v16
	v_add_f32_e32 v7, v13, v17
	v_add_f32_e32 v4, v4, v8
	v_add_f32_e32 v5, v5, v9
	v_cvt_pk_bf16_f32 v182, v162, v163
	v_cvt_pk_bf16_f32 v183, v164, v165
	v_cvt_pk_bf16_f32 v184, v166, v167
	v_cvt_pk_bf16_f32 v185, v168, v169
	v_cvt_pk_bf16_f32 v178, v146, v147
	s_nop 0
	v_add_f32_e32 v4, v6, v4
	v_add_f32_e32 v5, v7, v5
	v_cvt_pk_bf16_f32 v179, v148, v149
	v_cvt_pk_bf16_f32 v180, v150, v151
	v_cvt_pk_bf16_f32 v181, v152, v153
	v_cvt_pk_bf16_f32 v186, v170, v171
	v_cvt_pk_bf16_f32 v187, v172, v173
	s_nop 0
	v_add_f32_e32 v2, v4, v5
	v_add_f32_e32 v215, v215, v2
	v_cvt_pk_bf16_f32 v188, v174, v175
	v_cvt_pk_bf16_f32 v189, v176, v177
	v_cvt_pk_bf16_f32 v190, v154, v155
	v_cvt_pk_bf16_f32 v191, v156, v157
	v_cvt_pk_bf16_f32 v192, v158, v159
	v_cvt_pk_bf16_f32 v193, v160, v161

.LBB0_393:
	v_cndmask_b32_e64 v2, 0, 1, s[36:37]
	v_cmp_ne_u32_e64 s[8:9], 1, v2
	s_andn2_b64 vcc, exec, s[36:37]
	s_cbranch_vccnz .LBB0_404
	s_cmp_le_i32 s80, s64
	s_cbranch_scc1 .LBB0_396
	v_add_u32_e32 v2, s81, v218
	v_add_u32_e32 v4, 0x206e0, v2
	v_add_u32_e32 v6, 0x20760, v2
	ds_read2_b32 v[4:5], v4 offset1:1
	ds_read2_b32 v[6:7], v6 offset1:1
	v_add_u32_e32 v8, 0x206e8, v2
	v_add_u32_e32 v10, 0x20768, v2
	v_add_u32_e32 v12, 0x20700, v2
	v_add_u32_e32 v14, 0x20780, v2
	v_add_u32_e32 v16, 0x20708, v2
	v_add_u32_e32 v178, 0x20788, v2
	v_add_u32_e32 v180, 0x20720, v2
	v_add_u32_e32 v182, 0x207a0, v2
	v_add_u32_e32 v184, 0x20728, v2
	v_add_u32_e32 v186, 0x207a8, v2
	v_add_u32_e32 v188, 0x20740, v2
	v_add_u32_e32 v190, 0x207c0, v2
	v_add_u32_e32 v192, 0x20748, v2
	v_add_u32_e32 v2, 0x207c8, v2
	ds_read2_b32 v[8:9], v8 offset1:1
	ds_read2_b32 v[10:11], v10 offset1:1
	ds_read2_b32 v[12:13], v12 offset1:1
	ds_read2_b32 v[14:15], v14 offset1:1
	ds_read2_b32 v[16:17], v16 offset1:1
	ds_read2_b32 v[178:179], v178 offset1:1
	ds_read2_b32 v[180:181], v180 offset1:1
	ds_read2_b32 v[182:183], v182 offset1:1
	ds_read2_b32 v[184:185], v184 offset1:1
	ds_read2_b32 v[186:187], v186 offset1:1
	ds_read2_b32 v[188:189], v188 offset1:1
	ds_read2_b32 v[190:191], v190 offset1:1
	ds_read2_b32 v[192:193], v192 offset1:1
	s_waitcnt lgkmcnt(14)
	v_add_f32_e32 v162, v162, v4
	v_add_f32_e32 v163, v163, v5
	ds_read2_b32 v[4:5], v2 offset1:1
	s_waitcnt lgkmcnt(3)
	v_add_f32_e32 v174, v174, v188
	v_add_f32_e32 v175, v175, v189
	v_add_f32_e32 v172, v172, v184
	v_add_f32_e32 v173, v173, v185
	s_waitcnt lgkmcnt(1)
	v_add_f32_e32 v176, v176, v192
	v_add_f32_e32 v177, v177, v193
	v_add_f32_e32 v170, v170, v180
	v_add_f32_e32 v171, v171, v181
	v_add_f32_e32 v168, v168, v16
	v_add_f32_e32 v169, v169, v17
	v_add_f32_e32 v166, v166, v12
	v_add_f32_e32 v167, v167, v13
	v_add_f32_e32 v164, v164, v8
	v_add_f32_e32 v165, v165, v9
	s_waitcnt lgkmcnt(0)
	v_add_f32_e32 v160, v160, v4
	v_add_f32_e32 v161, v161, v5
	v_add_f32_e32 v158, v158, v190
	v_add_f32_e32 v159, v159, v191
	v_add_f32_e32 v156, v156, v186
	v_add_f32_e32 v157, v157, v187
	v_add_f32_e32 v154, v154, v182
	v_add_f32_e32 v155, v155, v183
	v_add_f32_e32 v152, v152, v178
	v_add_f32_e32 v153, v153, v179
	v_add_f32_e32 v150, v150, v14
	v_add_f32_e32 v151, v151, v15
	v_add_f32_e32 v148, v148, v10
	v_add_f32_e32 v149, v149, v11
	v_add_f32_e32 v146, v146, v6
	v_add_f32_e32 v147, v147, v7

.LBB0_399:
	s_and_b64 vcc, exec, s[24:25]
	s_cbranch_vccz .LBB0_403
	s_and_b64 vcc, exec, s[10:11]
	s_cbranch_vccnz .LBB0_402
	v_exp_f32_e64 v4, -v2
	s_nop 0
	v_mul_f32_e32 v128, v128, v4
	v_mul_f32_e32 v129, v129, v4
	v_mul_f32_e32 v126, v126, v4
	v_mul_f32_e32 v127, v127, v4
	v_mul_f32_e32 v124, v124, v4
	v_mul_f32_e32 v125, v125, v4
	v_mul_f32_e32 v122, v122, v4
	v_mul_f32_e32 v123, v123, v4
	v_mul_f32_e32 v120, v120, v4
	v_mul_f32_e32 v121, v121, v4
	v_mul_f32_e32 v118, v118, v4
	v_mul_f32_e32 v119, v119, v4
	v_mul_f32_e32 v116, v116, v4
	v_mul_f32_e32 v117, v117, v4
	v_mul_f32_e32 v114, v114, v4
	v_mul_f32_e32 v115, v115, v4
	v_mul_f32_e32 v96, v96, v4
	v_mul_f32_e32 v97, v97, v4
	v_mul_f32_e32 v94, v94, v4
	v_mul_f32_e32 v95, v95, v4
	v_mul_f32_e32 v92, v92, v4
	v_mul_f32_e32 v93, v93, v4
	v_mul_f32_e32 v90, v90, v4
	v_mul_f32_e32 v91, v91, v4
	v_mul_f32_e32 v88, v88, v4
	v_mul_f32_e32 v89, v89, v4
	v_mul_f32_e32 v86, v86, v4
	v_mul_f32_e32 v87, v87, v4
	v_mul_f32_e32 v84, v84, v4
	v_mul_f32_e32 v85, v85, v4
	v_mul_f32_e32 v82, v82, v4
	v_mul_f32_e32 v83, v83, v4
	v_mul_f32_e32 v64, v64, v4
	v_mul_f32_e32 v65, v65, v4
	v_mul_f32_e32 v62, v62, v4
	v_mul_f32_e32 v63, v63, v4
	v_mul_f32_e32 v60, v60, v4
	v_mul_f32_e32 v61, v61, v4
	v_mul_f32_e32 v58, v58, v4
	v_mul_f32_e32 v59, v59, v4
	v_mul_f32_e32 v56, v56, v4
	v_mul_f32_e32 v57, v57, v4
	v_mul_f32_e32 v54, v54, v4
	v_mul_f32_e32 v55, v55, v4
	v_mul_f32_e32 v52, v52, v4
	v_mul_f32_e32 v53, v53, v4
	v_mul_f32_e32 v50, v50, v4
	v_mul_f32_e32 v51, v51, v4
	v_mul_f32_e32 v32, v32, v4
	v_mul_f32_e32 v33, v33, v4
	v_mul_f32_e32 v30, v30, v4
	v_mul_f32_e32 v31, v31, v4
	v_mul_f32_e32 v28, v28, v4
	v_mul_f32_e32 v29, v29, v4
	v_mul_f32_e32 v26, v26, v4
	v_mul_f32_e32 v27, v27, v4
	v_mul_f32_e32 v24, v24, v4
	v_mul_f32_e32 v25, v25, v4
	v_mul_f32_e32 v22, v22, v4
	v_mul_f32_e32 v23, v23, v4
	v_mul_f32_e32 v20, v20, v4
	v_mul_f32_e32 v21, v21, v4
	v_mul_f32_e32 v18, v18, v4
	v_mul_f32_e32 v19, v19, v4
	v_mul_f32_e32 v214, v214, v4
.LBB0_402:
	v_sub_f32_e32 v162, v162, v2
	v_sub_f32_e32 v163, v163, v2
	v_sub_f32_e32 v146, v146, v2
	v_sub_f32_e32 v147, v147, v2
	v_sub_f32_e32 v164, v164, v2
	v_sub_f32_e32 v165, v165, v2
	v_sub_f32_e32 v148, v148, v2
	v_sub_f32_e32 v149, v149, v2
	v_sub_f32_e32 v166, v166, v2
	v_sub_f32_e32 v167, v167, v2
	v_sub_f32_e32 v150, v150, v2
	v_sub_f32_e32 v151, v151, v2
	v_sub_f32_e32 v168, v168, v2
	v_sub_f32_e32 v169, v169, v2
	v_sub_f32_e32 v152, v152, v2
	v_sub_f32_e32 v153, v153, v2
	v_sub_f32_e32 v170, v170, v2
	v_sub_f32_e32 v171, v171, v2
	v_sub_f32_e32 v154, v154, v2
	v_sub_f32_e32 v155, v155, v2
	v_sub_f32_e32 v172, v172, v2
	v_sub_f32_e32 v173, v173, v2
	v_sub_f32_e32 v156, v156, v2
	v_sub_f32_e32 v157, v157, v2
	v_sub_f32_e32 v174, v174, v2
	v_sub_f32_e32 v175, v175, v2
	v_sub_f32_e32 v158, v158, v2
	v_sub_f32_e32 v159, v159, v2
	v_sub_f32_e32 v176, v176, v2
	v_sub_f32_e32 v177, v177, v2
	v_sub_f32_e32 v160, v160, v2
	v_sub_f32_e32 v161, v161, v2
	v_add_f32_e32 v219, v219, v2
.LBB0_403:
	v_exp_f32_e32 v162, v162
	v_exp_f32_e32 v146, v146
	v_exp_f32_e32 v163, v163
	v_exp_f32_e32 v147, v147
	v_exp_f32_e32 v164, v164
	v_exp_f32_e32 v148, v148
	v_exp_f32_e32 v165, v165
	v_exp_f32_e32 v149, v149
	v_exp_f32_e32 v166, v166
	v_exp_f32_e32 v150, v150
	v_exp_f32_e32 v167, v167
	v_exp_f32_e32 v151, v151
	v_exp_f32_e32 v168, v168
	v_exp_f32_e32 v152, v152
	v_exp_f32_e32 v169, v169
	v_exp_f32_e32 v153, v153
	v_exp_f32_e32 v170, v170
	v_exp_f32_e32 v154, v154
	v_exp_f32_e32 v171, v171
	v_exp_f32_e32 v155, v155
	v_exp_f32_e32 v172, v172
	v_exp_f32_e32 v156, v156
	v_exp_f32_e32 v173, v173
	v_exp_f32_e32 v157, v157
	v_exp_f32_e32 v174, v174
	v_exp_f32_e32 v158, v158
	v_exp_f32_e32 v175, v175
	v_exp_f32_e32 v176, v176
	v_exp_f32_e32 v160, v160
	v_exp_f32_e32 v177, v177
	v_exp_f32_e32 v161, v161
	v_exp_f32_e32 v159, v159
	v_add_f32_e32 v4, v156, v172
	v_add_f32_e32 v5, v157, v173
	v_add_f32_e32 v6, v148, v164
	v_add_f32_e32 v7, v149, v165
	v_add_f32_e32 v8, v160, v176
	v_add_f32_e32 v9, v161, v177
	v_add_f32_e32 v10, v152, v168
	v_add_f32_e32 v11, v153, v169
	v_add_f32_e32 v12, v154, v170
	v_add_f32_e32 v13, v155, v171
	v_add_f32_e32 v14, v146, v162
	v_add_f32_e32 v15, v147, v163
	v_add_f32_e32 v16, v158, v174
	v_add_f32_e32 v17, v159, v175
	v_add_f32_e32 v178, v150, v166
	v_add_f32_e32 v179, v151, v167
	v_add_f32_e32 v12, v14, v12
	v_add_f32_e32 v13, v15, v13
	v_add_f32_e32 v16, v178, v16
	v_add_f32_e32 v17, v179, v17
	v_add_f32_e32 v8, v10, v8
	v_add_f32_e32 v9, v11, v9
	v_add_f32_e32 v4, v6, v4
	v_add_f32_e32 v5, v7, v5
	v_add_f32_e32 v6, v12, v16
	v_add_f32_e32 v7, v13, v17
	v_add_f32_e32 v4, v4, v8
	v_add_f32_e32 v5, v5, v9
	v_cvt_pk_bf16_f32 v182, v162, v163
	v_cvt_pk_bf16_f32 v183, v164, v165
	v_cvt_pk_bf16_f32 v184, v166, v167
	v_cvt_pk_bf16_f32 v185, v168, v169
	v_cvt_pk_bf16_f32 v178, v146, v147
	s_nop 0
	v_add_f32_e32 v4, v6, v4
	v_add_f32_e32 v5, v7, v5
	v_cvt_pk_bf16_f32 v179, v148, v149
	v_cvt_pk_bf16_f32 v180, v150, v151
	v_cvt_pk_bf16_f32 v181, v152, v153
	v_cvt_pk_bf16_f32 v186, v170, v171
	v_cvt_pk_bf16_f32 v187, v172, v173
	s_nop 0
	v_add_f32_e32 v2, v4, v5
	v_add_f32_e32 v214, v214, v2
	v_cvt_pk_bf16_f32 v188, v174, v175
	v_cvt_pk_bf16_f32 v189, v176, v177
	v_cvt_pk_bf16_f32 v190, v154, v155
	v_cvt_pk_bf16_f32 v191, v156, v157
	v_cvt_pk_bf16_f32 v192, v158, v159
	v_cvt_pk_bf16_f32 v193, v160, v161

.LBB0_410:
	s_waitcnt vmcnt(0)
	s_waitcnt lgkmcnt(0)
	s_barrier
	v_cndmask_b32_e64 v2, 0, 1, s[58:59]
	v_cmp_ne_u32_e64 s[8:9], 1, v2
	s_andn2_b64 vcc, exec, s[58:59]
	s_cbranch_vccnz .LBB0_416
	v_readlane_b32 s6, v255, 32
	v_readlane_b32 s7, v255, 33
	s_andn2_b64 vcc, exec, s[6:7]
	v_mov_b32_e32 v219, v221
	s_cbranch_vccnz .LBB0_413
	v_or_b32_e32 v2, s97, v217
	v_sub_u32_e32 v2, 0xc0, v2
	s_add_i32 s6, 0, 0x20000
	v_lshlrev_b32_e32 v2, 2, v2
	v_lshlrev_b32_e32 v4, 2, v196
	v_add3_u32 v2, s6, v2, v4
	ds_read2_b32 v[4:5], v2 offset0:184 offset1:185
	ds_read2_b32 v[6:7], v2 offset0:186 offset1:187
	ds_read2_b32 v[8:9], v2 offset0:192 offset1:193
	ds_read2_b32 v[10:11], v2 offset0:194 offset1:195
	ds_read2_b32 v[12:13], v2 offset0:200 offset1:201
	ds_read2_b32 v[14:15], v2 offset0:202 offset1:203
	ds_read2_b32 v[16:17], v2 offset0:208 offset1:209
	ds_read2_b32 v[178:179], v2 offset0:210 offset1:211
	ds_read2_b32 v[180:181], v2 offset0:216 offset1:217
	ds_read2_b32 v[182:183], v2 offset0:218 offset1:219
	ds_read2_b32 v[184:185], v2 offset0:224 offset1:225
	ds_read2_b32 v[186:187], v2 offset0:226 offset1:227
	s_waitcnt lgkmcnt(4)
	v_add_f32_e32 v176, v176, v178
	v_add_f32_e32 v177, v177, v179
	v_add_f32_e32 v174, v174, v16
	v_add_f32_e32 v175, v175, v17
	v_add_f32_e32 v172, v172, v14
	v_add_f32_e32 v173, v173, v15
	v_add_f32_e32 v170, v170, v12
	v_add_f32_e32 v171, v171, v13
	ds_read2_b32 v[12:13], v2 offset0:232 offset1:233
	ds_read2_b32 v[14:15], v2 offset0:234 offset1:235
	ds_read2_b32 v[16:17], v2 offset0:240 offset1:241
	ds_read2_b32 v[178:179], v2 offset0:242 offset1:243
	v_add_f32_e32 v168, v168, v10
	v_add_f32_e32 v169, v169, v11
	v_add_f32_e32 v166, v166, v8
	v_add_f32_e32 v167, v167, v9
	v_add_f32_e32 v164, v164, v6
	v_add_f32_e32 v165, v165, v7
	v_add_f32_e32 v162, v162, v4
	v_add_f32_e32 v163, v163, v5
	s_waitcnt lgkmcnt(0)
	v_add_f32_e32 v160, v160, v178
	v_add_f32_e32 v161, v161, v179
	v_add_f32_e32 v158, v158, v16
	v_add_f32_e32 v159, v159, v17
	v_add_f32_e32 v156, v156, v14
	v_add_f32_e32 v157, v157, v15
	v_add_f32_e32 v154, v154, v12
	v_add_f32_e32 v155, v155, v13
	v_add_f32_e32 v152, v152, v186
	v_add_f32_e32 v153, v153, v187
	v_add_f32_e32 v150, v150, v184
	v_add_f32_e32 v151, v151, v185
	v_add_f32_e32 v148, v148, v182
	v_add_f32_e32 v149, v149, v183
	v_add_f32_e32 v146, v146, v180
	v_add_f32_e32 v147, v147, v181
.LBB0_413:
	s_nop 0
	v_max_f32_e32 v5, v147, v147
	v_max_f32_e32 v6, v146, v146
	v_max3_f32 v2, v162, v163, v164
	v_max3_f32 v4, v170, v171, v172
	v_max_f32_e32 v5, v6, v5
	v_max3_f32 v6, v154, v155, v156
	v_max3_f32 v2, v2, v165, v166
	v_max3_f32 v4, v4, v173, v174
	v_max3_f32 v5, v5, v148, v149
	v_max3_f32 v6, v6, v157, v158
	v_max3_f32 v2, v2, v167, v168
	v_max3_f32 v4, v4, v175, v176
	v_max3_f32 v5, v5, v150, v151
	v_max3_f32 v6, v6, v159, v160
	v_max3_f32 v2, v2, v169, v4
	v_max3_f32 v4, v5, v152, v153
	v_max3_f32 v4, v4, v6, v161
	v_max3_f32 v2, v2, v177, v4
	v_mov_b32_e32 v4, v2
	s_nop 1
	v_permlane32_swap_b32_e32 v2, v4
	v_max_f32_e32 v4, v4, v4
	v_max_f32_e32 v2, v2, v2
	v_max_f32_e32 v2, v2, v4
	v_cmp_lt_f32_e32 vcc, s0, v2
	s_cbranch_vccz .LBB0_415
	v_max_f32_e32 v2, v2, v2
	v_max_f32_e32 v2, 0, v2
	v_exp_f32_e64 v4, -v2
	v_sub_f32_e32 v162, v162, v2
	v_sub_f32_e32 v163, v163, v2
	v_sub_f32_e32 v146, v146, v2
	v_sub_f32_e32 v147, v147, v2
	v_sub_f32_e32 v164, v164, v2
	v_sub_f32_e32 v165, v165, v2
	v_mul_f32_e32 v144, v144, v4
	v_mul_f32_e32 v145, v145, v4
	v_mul_f32_e32 v142, v142, v4
	v_mul_f32_e32 v143, v143, v4
	v_mul_f32_e32 v140, v140, v4
	v_mul_f32_e32 v141, v141, v4
	v_mul_f32_e32 v138, v138, v4
	v_mul_f32_e32 v139, v139, v4
	v_mul_f32_e32 v136, v136, v4
	v_mul_f32_e32 v137, v137, v4
	v_mul_f32_e32 v134, v134, v4
	v_mul_f32_e32 v135, v135, v4
	v_mul_f32_e32 v132, v132, v4
	v_mul_f32_e32 v133, v133, v4
	v_mul_f32_e32 v130, v130, v4
	v_mul_f32_e32 v131, v131, v4
	v_mul_f32_e32 v112, v112, v4
	v_mul_f32_e32 v113, v113, v4
	v_mul_f32_e32 v110, v110, v4
	v_mul_f32_e32 v111, v111, v4
	v_mul_f32_e32 v108, v108, v4
	v_mul_f32_e32 v109, v109, v4
	v_mul_f32_e32 v106, v106, v4
	v_mul_f32_e32 v107, v107, v4
	v_mul_f32_e32 v104, v104, v4
	v_mul_f32_e32 v105, v105, v4
	v_mul_f32_e32 v102, v102, v4
	v_mul_f32_e32 v103, v103, v4
	v_mul_f32_e32 v100, v100, v4
	v_mul_f32_e32 v101, v101, v4
	v_mul_f32_e32 v98, v98, v4
	v_mul_f32_e32 v99, v99, v4
	v_mul_f32_e32 v80, v80, v4
	v_mul_f32_e32 v81, v81, v4
	v_mul_f32_e32 v78, v78, v4
	v_mul_f32_e32 v79, v79, v4
	v_mul_f32_e32 v76, v76, v4
	v_mul_f32_e32 v77, v77, v4
	v_mul_f32_e32 v74, v74, v4
	v_mul_f32_e32 v75, v75, v4
	v_mul_f32_e32 v72, v72, v4
	v_mul_f32_e32 v73, v73, v4
	v_mul_f32_e32 v70, v70, v4
	v_mul_f32_e32 v71, v71, v4
	v_mul_f32_e32 v68, v68, v4
	v_mul_f32_e32 v69, v69, v4
	v_mul_f32_e32 v66, v66, v4
	v_mul_f32_e32 v67, v67, v4
	v_mul_f32_e32 v48, v48, v4
	v_mul_f32_e32 v49, v49, v4
	v_mul_f32_e32 v46, v46, v4
	v_mul_f32_e32 v47, v47, v4
	v_mul_f32_e32 v44, v44, v4
	v_mul_f32_e32 v45, v45, v4
	v_mul_f32_e32 v42, v42, v4
	v_mul_f32_e32 v43, v43, v4
	v_mul_f32_e32 v40, v40, v4
	v_mul_f32_e32 v41, v41, v4
	v_mul_f32_e32 v38, v38, v4
	v_mul_f32_e32 v39, v39, v4
	v_mul_f32_e32 v36, v36, v4
	v_mul_f32_e32 v37, v37, v4
	v_mul_f32_e32 v34, v34, v4
	v_mul_f32_e32 v35, v35, v4
	v_sub_f32_e32 v148, v148, v2
	v_sub_f32_e32 v149, v149, v2
	v_sub_f32_e32 v166, v166, v2
	v_sub_f32_e32 v167, v167, v2
	v_sub_f32_e32 v150, v150, v2
	v_sub_f32_e32 v151, v151, v2
	v_sub_f32_e32 v168, v168, v2
	v_sub_f32_e32 v169, v169, v2
	v_sub_f32_e32 v152, v152, v2
	v_sub_f32_e32 v153, v153, v2
	v_sub_f32_e32 v170, v170, v2
	v_sub_f32_e32 v171, v171, v2
	v_sub_f32_e32 v154, v154, v2
	v_sub_f32_e32 v155, v155, v2
	v_sub_f32_e32 v172, v172, v2
	v_sub_f32_e32 v173, v173, v2
	v_sub_f32_e32 v156, v156, v2
	v_sub_f32_e32 v157, v157, v2
	v_sub_f32_e32 v174, v174, v2
	v_sub_f32_e32 v175, v175, v2
	v_sub_f32_e32 v158, v158, v2
	v_sub_f32_e32 v159, v159, v2
	v_sub_f32_e32 v176, v176, v2
	v_sub_f32_e32 v177, v177, v2
	v_sub_f32_e32 v160, v160, v2
	v_sub_f32_e32 v161, v161, v2
	v_mul_f32_e32 v215, v215, v4
.LBB0_415:
	v_exp_f32_e32 v4, v162
	v_exp_f32_e32 v6, v146
	v_exp_f32_e32 v5, v163
	v_exp_f32_e32 v7, v147
	v_exp_f32_e32 v8, v164
	v_exp_f32_e32 v10, v148
	v_exp_f32_e32 v9, v165
	v_exp_f32_e32 v11, v149
	v_exp_f32_e32 v12, v166
	v_exp_f32_e32 v14, v150
	v_exp_f32_e32 v13, v167
	v_exp_f32_e32 v15, v151
	v_exp_f32_e32 v16, v168
	v_exp_f32_e32 v146, v152
	v_exp_f32_e32 v17, v169
	v_exp_f32_e32 v147, v153
	v_exp_f32_e32 v148, v170
	v_exp_f32_e32 v150, v154
	v_exp_f32_e32 v149, v171
	v_exp_f32_e32 v151, v155
	v_exp_f32_e32 v152, v172
	v_exp_f32_e32 v154, v156
	v_exp_f32_e32 v153, v173
	v_exp_f32_e32 v155, v157
	v_exp_f32_e32 v156, v174
	v_exp_f32_e32 v158, v158
	v_exp_f32_e32 v157, v175
	v_exp_f32_e32 v162, v176
	v_exp_f32_e32 v160, v160
	v_exp_f32_e32 v163, v177
	v_exp_f32_e32 v161, v161
	v_exp_f32_e32 v159, v159
	v_add_f32_e32 v164, v154, v152
	v_add_f32_e32 v165, v155, v153
	v_add_f32_e32 v166, v10, v8
	v_add_f32_e32 v167, v11, v9
	v_add_f32_e32 v168, v160, v162
	v_add_f32_e32 v169, v161, v163
	v_add_f32_e32 v170, v146, v16
	v_add_f32_e32 v171, v147, v17
	v_add_f32_e32 v172, v150, v148
	v_add_f32_e32 v173, v151, v149
	v_add_f32_e32 v174, v6, v4
	v_add_f32_e32 v175, v7, v5
	v_add_f32_e32 v176, v158, v156
	v_add_f32_e32 v177, v159, v157
	v_add_f32_e32 v178, v14, v12
	v_add_f32_e32 v179, v15, v13
	v_add_f32_e32 v172, v174, v172
	v_add_f32_e32 v173, v175, v173
	v_add_f32_e32 v176, v178, v176
	v_add_f32_e32 v177, v179, v177
	v_add_f32_e32 v168, v170, v168
	v_add_f32_e32 v169, v171, v169
	v_add_f32_e32 v164, v166, v164
	v_add_f32_e32 v165, v167, v165
	v_add_f32_e32 v166, v172, v176
	v_add_f32_e32 v167, v173, v177
	v_add_f32_e32 v164, v164, v168
	v_add_f32_e32 v165, v165, v169
	v_cvt_pk_bf16_f32 v182, v4, v5
	v_cvt_pk_bf16_f32 v183, v8, v9
	v_cvt_pk_bf16_f32 v184, v12, v13
	v_cvt_pk_bf16_f32 v185, v16, v17
	v_cvt_pk_bf16_f32 v178, v6, v7
	s_nop 0
	v_add_f32_e32 v164, v166, v164
	v_add_f32_e32 v165, v167, v165
	v_cvt_pk_bf16_f32 v179, v10, v11
	v_cvt_pk_bf16_f32 v180, v14, v15
	v_cvt_pk_bf16_f32 v181, v146, v147
	v_cvt_pk_bf16_f32 v186, v148, v149
	v_cvt_pk_bf16_f32 v187, v152, v153
	s_nop 0
	v_add_f32_e32 v2, v164, v165
	v_add_f32_e32 v215, v215, v2
	v_cvt_pk_bf16_f32 v188, v156, v157
	v_cvt_pk_bf16_f32 v189, v162, v163
	v_cvt_pk_bf16_f32 v190, v150, v151
	v_cvt_pk_bf16_f32 v191, v154, v155
	v_cvt_pk_bf16_f32 v192, v158, v159
	v_cvt_pk_bf16_f32 v193, v160, v161
	s_branch .LBB0_417

.LBB0_422:
	v_sub_f32_e32 v162, v162, v2
	v_sub_f32_e32 v163, v163, v2
	v_sub_f32_e32 v146, v146, v2
	v_sub_f32_e32 v147, v147, v2
	v_sub_f32_e32 v164, v164, v2
	v_sub_f32_e32 v165, v165, v2
	v_sub_f32_e32 v148, v148, v2
	v_sub_f32_e32 v149, v149, v2
	v_sub_f32_e32 v166, v166, v2
	v_sub_f32_e32 v167, v167, v2
	v_sub_f32_e32 v150, v150, v2
	v_sub_f32_e32 v151, v151, v2
	v_sub_f32_e32 v168, v168, v2
	v_sub_f32_e32 v169, v169, v2
	v_sub_f32_e32 v152, v152, v2
	v_sub_f32_e32 v153, v153, v2
	v_sub_f32_e32 v170, v170, v2
	v_sub_f32_e32 v171, v171, v2
	v_sub_f32_e32 v154, v154, v2
	v_sub_f32_e32 v155, v155, v2
	v_sub_f32_e32 v172, v172, v2
	v_sub_f32_e32 v173, v173, v2
	v_sub_f32_e32 v156, v156, v2
	v_sub_f32_e32 v157, v157, v2
	v_sub_f32_e32 v174, v174, v2
	v_sub_f32_e32 v175, v175, v2
	v_sub_f32_e32 v158, v158, v2
	v_sub_f32_e32 v159, v159, v2
	v_sub_f32_e32 v176, v176, v2
	v_sub_f32_e32 v177, v177, v2
	v_sub_f32_e32 v160, v160, v2
	v_sub_f32_e32 v161, v161, v2
	v_add_f32_e32 v218, v218, v2
.LBB0_423:
	v_exp_f32_e32 v162, v162
	v_exp_f32_e32 v146, v146
	v_exp_f32_e32 v163, v163
	v_exp_f32_e32 v147, v147
	v_exp_f32_e32 v164, v164
	v_exp_f32_e32 v148, v148
	v_exp_f32_e32 v165, v165
	v_exp_f32_e32 v149, v149
	v_exp_f32_e32 v166, v166
	v_exp_f32_e32 v150, v150
	v_exp_f32_e32 v167, v167
	v_exp_f32_e32 v151, v151
	v_exp_f32_e32 v168, v168
	v_exp_f32_e32 v152, v152
	v_exp_f32_e32 v169, v169
	v_exp_f32_e32 v153, v153
	v_exp_f32_e32 v170, v170
	v_exp_f32_e32 v154, v154
	v_exp_f32_e32 v171, v171
	v_exp_f32_e32 v155, v155
	v_exp_f32_e32 v172, v172
	v_exp_f32_e32 v156, v156
	v_exp_f32_e32 v173, v173
	v_exp_f32_e32 v157, v157
	v_exp_f32_e32 v174, v174
	v_exp_f32_e32 v158, v158
	v_exp_f32_e32 v175, v175
	v_exp_f32_e32 v176, v176
	v_exp_f32_e32 v160, v160
	v_exp_f32_e32 v177, v177
	v_exp_f32_e32 v161, v161
	v_exp_f32_e32 v159, v159
	v_add_f32_e32 v4, v156, v172
	v_add_f32_e32 v5, v157, v173
	v_add_f32_e32 v6, v148, v164
	v_add_f32_e32 v7, v149, v165
	v_add_f32_e32 v8, v160, v176
	v_add_f32_e32 v9, v161, v177
	v_add_f32_e32 v10, v152, v168
	v_add_f32_e32 v11, v153, v169
	v_add_f32_e32 v12, v154, v170
	v_add_f32_e32 v13, v155, v171
	v_add_f32_e32 v14, v146, v162
	v_add_f32_e32 v15, v147, v163
	v_add_f32_e32 v16, v158, v174
	v_add_f32_e32 v17, v159, v175
	v_add_f32_e32 v178, v150, v166
	v_add_f32_e32 v179, v151, v167
	v_add_f32_e32 v12, v14, v12
	v_add_f32_e32 v13, v15, v13
	v_add_f32_e32 v16, v178, v16
	v_add_f32_e32 v17, v179, v17
	v_add_f32_e32 v8, v10, v8
	v_add_f32_e32 v9, v11, v9
	v_add_f32_e32 v4, v6, v4
	v_add_f32_e32 v5, v7, v5
	v_add_f32_e32 v6, v12, v16
	v_add_f32_e32 v7, v13, v17
	v_add_f32_e32 v4, v4, v8
	v_add_f32_e32 v5, v5, v9
	v_cvt_pk_bf16_f32 v178, v162, v163
	v_cvt_pk_bf16_f32 v179, v164, v165
	v_cvt_pk_bf16_f32 v180, v166, v167
	v_cvt_pk_bf16_f32 v181, v168, v169
	v_cvt_pk_bf16_f32 v182, v146, v147
	s_nop 0
	v_add_f32_e32 v4, v6, v4
	v_add_f32_e32 v5, v7, v5
	v_cvt_pk_bf16_f32 v183, v148, v149
	v_cvt_pk_bf16_f32 v184, v150, v151
	v_cvt_pk_bf16_f32 v185, v152, v153
	v_cvt_pk_bf16_f32 v186, v170, v171
	v_cvt_pk_bf16_f32 v187, v172, v173
	s_nop 0
	v_add_f32_e32 v2, v4, v5
	v_add_f32_e32 v215, v215, v2
	v_cvt_pk_bf16_f32 v188, v174, v175
	v_cvt_pk_bf16_f32 v189, v176, v177
	v_cvt_pk_bf16_f32 v190, v154, v155
	v_cvt_pk_bf16_f32 v191, v156, v157
	v_cvt_pk_bf16_f32 v192, v158, v159
	v_cvt_pk_bf16_f32 v193, v160, v161

.LBB0_432:
	s_waitcnt lgkmcnt(0)
	s_barrier
	v_cndmask_b32_e64 v2, 0, 1, s[10:11]
	v_cmp_ne_u32_e64 s[8:9], 1, v2
	s_andn2_b64 vcc, exec, s[10:11]
	s_cbranch_vccnz .LBB0_443
	s_cmp_le_i32 s65, s64
	s_cbranch_scc1 .LBB0_435
	v_add_u32_e32 v2, s38, v216
	v_add_u32_e32 v4, 0x206e0, v2
	v_add_u32_e32 v6, 0x20760, v2
	ds_read2_b32 v[4:5], v4 offset1:1
	ds_read2_b32 v[6:7], v6 offset1:1
	v_add_u32_e32 v8, 0x206e8, v2
	v_add_u32_e32 v10, 0x20768, v2
	v_add_u32_e32 v12, 0x20700, v2
	v_add_u32_e32 v14, 0x20780, v2
	v_add_u32_e32 v16, 0x20708, v2
	v_add_u32_e32 v178, 0x20788, v2
	v_add_u32_e32 v180, 0x20720, v2
	v_add_u32_e32 v182, 0x207a0, v2
	v_add_u32_e32 v184, 0x20728, v2
	v_add_u32_e32 v186, 0x207a8, v2
	v_add_u32_e32 v188, 0x20740, v2
	v_add_u32_e32 v190, 0x207c0, v2
	v_add_u32_e32 v192, 0x20748, v2
	v_add_u32_e32 v2, 0x207c8, v2
	ds_read2_b32 v[8:9], v8 offset1:1
	ds_read2_b32 v[10:11], v10 offset1:1
	ds_read2_b32 v[12:13], v12 offset1:1
	ds_read2_b32 v[14:15], v14 offset1:1
	ds_read2_b32 v[16:17], v16 offset1:1
	ds_read2_b32 v[178:179], v178 offset1:1
	ds_read2_b32 v[180:181], v180 offset1:1
	ds_read2_b32 v[182:183], v182 offset1:1
	ds_read2_b32 v[184:185], v184 offset1:1
	ds_read2_b32 v[186:187], v186 offset1:1
	ds_read2_b32 v[188:189], v188 offset1:1
	ds_read2_b32 v[190:191], v190 offset1:1
	ds_read2_b32 v[192:193], v192 offset1:1
	s_waitcnt lgkmcnt(14)
	v_add_f32_e32 v162, v162, v4
	v_add_f32_e32 v163, v163, v5
	ds_read2_b32 v[4:5], v2 offset1:1
	s_waitcnt lgkmcnt(3)
	v_add_f32_e32 v174, v174, v188
	v_add_f32_e32 v175, v175, v189
	v_add_f32_e32 v172, v172, v184
	v_add_f32_e32 v173, v173, v185
	s_waitcnt lgkmcnt(1)
	v_add_f32_e32 v176, v176, v192
	v_add_f32_e32 v177, v177, v193
	v_add_f32_e32 v170, v170, v180
	v_add_f32_e32 v171, v171, v181
	v_add_f32_e32 v168, v168, v16
	v_add_f32_e32 v169, v169, v17
	v_add_f32_e32 v166, v166, v12
	v_add_f32_e32 v167, v167, v13
	v_add_f32_e32 v164, v164, v8
	v_add_f32_e32 v165, v165, v9
	s_waitcnt lgkmcnt(0)
	v_add_f32_e32 v160, v160, v4
	v_add_f32_e32 v161, v161, v5
	v_add_f32_e32 v158, v158, v190
	v_add_f32_e32 v159, v159, v191
	v_add_f32_e32 v156, v156, v186
	v_add_f32_e32 v157, v157, v187
	v_add_f32_e32 v154, v154, v182
	v_add_f32_e32 v155, v155, v183
	v_add_f32_e32 v152, v152, v178
	v_add_f32_e32 v153, v153, v179
	v_add_f32_e32 v150, v150, v14
	v_add_f32_e32 v151, v151, v15
	v_add_f32_e32 v148, v148, v10
	v_add_f32_e32 v149, v149, v11
	v_add_f32_e32 v146, v146, v6
	v_add_f32_e32 v147, v147, v7

.LBB0_441:
	v_sub_f32_e32 v162, v162, v2
	v_sub_f32_e32 v163, v163, v2
	v_sub_f32_e32 v146, v146, v2
	v_sub_f32_e32 v147, v147, v2
	v_sub_f32_e32 v164, v164, v2
	v_sub_f32_e32 v165, v165, v2
	v_sub_f32_e32 v148, v148, v2
	v_sub_f32_e32 v149, v149, v2
	v_sub_f32_e32 v166, v166, v2
	v_sub_f32_e32 v167, v167, v2
	v_sub_f32_e32 v150, v150, v2
	v_sub_f32_e32 v151, v151, v2
	v_sub_f32_e32 v168, v168, v2
	v_sub_f32_e32 v169, v169, v2
	v_sub_f32_e32 v152, v152, v2
	v_sub_f32_e32 v153, v153, v2
	v_sub_f32_e32 v170, v170, v2
	v_sub_f32_e32 v171, v171, v2
	v_sub_f32_e32 v154, v154, v2
	v_sub_f32_e32 v155, v155, v2
	v_sub_f32_e32 v172, v172, v2
	v_sub_f32_e32 v173, v173, v2
	v_sub_f32_e32 v156, v156, v2
	v_sub_f32_e32 v157, v157, v2
	v_sub_f32_e32 v174, v174, v2
	v_sub_f32_e32 v175, v175, v2
	v_sub_f32_e32 v158, v158, v2
	v_sub_f32_e32 v159, v159, v2
	v_sub_f32_e32 v176, v176, v2
	v_sub_f32_e32 v177, v177, v2
	v_sub_f32_e32 v160, v160, v2
	v_sub_f32_e32 v161, v161, v2
	v_add_f32_e32 v217, v217, v2
.LBB0_442:
	v_exp_f32_e32 v162, v162
	v_exp_f32_e32 v146, v146
	v_exp_f32_e32 v163, v163
	v_exp_f32_e32 v147, v147
	v_exp_f32_e32 v164, v164
	v_exp_f32_e32 v148, v148
	v_exp_f32_e32 v165, v165
	v_exp_f32_e32 v149, v149
	v_exp_f32_e32 v166, v166
	v_exp_f32_e32 v150, v150
	v_exp_f32_e32 v167, v167
	v_exp_f32_e32 v151, v151
	v_exp_f32_e32 v168, v168
	v_exp_f32_e32 v152, v152
	v_exp_f32_e32 v169, v169
	v_exp_f32_e32 v153, v153
	v_exp_f32_e32 v170, v170
	v_exp_f32_e32 v154, v154
	v_exp_f32_e32 v171, v171
	v_exp_f32_e32 v155, v155
	v_exp_f32_e32 v172, v172
	v_exp_f32_e32 v156, v156
	v_exp_f32_e32 v173, v173
	v_exp_f32_e32 v157, v157
	v_exp_f32_e32 v174, v174
	v_exp_f32_e32 v158, v158
	v_exp_f32_e32 v175, v175
	v_exp_f32_e32 v176, v176
	v_exp_f32_e32 v160, v160
	v_exp_f32_e32 v177, v177
	v_exp_f32_e32 v161, v161
	v_exp_f32_e32 v159, v159
	v_add_f32_e32 v4, v156, v172
	v_add_f32_e32 v5, v157, v173
	v_add_f32_e32 v6, v148, v164
	v_add_f32_e32 v7, v149, v165
	v_add_f32_e32 v8, v160, v176
	v_add_f32_e32 v9, v161, v177
	v_add_f32_e32 v10, v152, v168
	v_add_f32_e32 v11, v153, v169
	v_add_f32_e32 v12, v154, v170
	v_add_f32_e32 v13, v155, v171
	v_add_f32_e32 v14, v146, v162
	v_add_f32_e32 v15, v147, v163
	v_add_f32_e32 v16, v158, v174
	v_add_f32_e32 v17, v159, v175
	v_add_f32_e32 v178, v150, v166
	v_add_f32_e32 v179, v151, v167
	v_add_f32_e32 v12, v14, v12
	v_add_f32_e32 v13, v15, v13
	v_add_f32_e32 v16, v178, v16
	v_add_f32_e32 v17, v179, v17
	v_add_f32_e32 v8, v10, v8
	v_add_f32_e32 v9, v11, v9
	v_add_f32_e32 v4, v6, v4
	v_add_f32_e32 v5, v7, v5
	v_add_f32_e32 v6, v12, v16
	v_add_f32_e32 v7, v13, v17
	v_add_f32_e32 v4, v4, v8
	v_add_f32_e32 v5, v5, v9
	v_cvt_pk_bf16_f32 v178, v162, v163
	v_cvt_pk_bf16_f32 v179, v164, v165
	v_cvt_pk_bf16_f32 v180, v166, v167
	v_cvt_pk_bf16_f32 v181, v168, v169
	v_cvt_pk_bf16_f32 v182, v146, v147
	s_nop 0
	v_add_f32_e32 v4, v6, v4
	v_add_f32_e32 v5, v7, v5
	v_cvt_pk_bf16_f32 v183, v148, v149
	v_cvt_pk_bf16_f32 v184, v150, v151
	v_cvt_pk_bf16_f32 v185, v152, v153
	v_cvt_pk_bf16_f32 v186, v170, v171
	v_cvt_pk_bf16_f32 v187, v172, v173
	s_nop 0
	v_add_f32_e32 v2, v4, v5
	v_add_f32_e32 v214, v214, v2
	v_cvt_pk_bf16_f32 v188, v174, v175
	v_cvt_pk_bf16_f32 v189, v176, v177
	v_cvt_pk_bf16_f32 v190, v154, v155
	v_cvt_pk_bf16_f32 v191, v156, v157
	v_cvt_pk_bf16_f32 v192, v158, v159
	v_cvt_pk_bf16_f32 v193, v160, v161

.LBB0_451:
	s_waitcnt lgkmcnt(0)
	s_barrier
	s_and_b64 vcc, exec, s[8:9]
	s_cbranch_vccnz .LBB0_424
	s_cmp_le_i32 s65, s64
	s_cbranch_scc1 .LBB0_454
	v_add_u32_e32 v2, s38, v216
	v_add_u32_e32 v4, 0x206e0, v2
	v_add_u32_e32 v6, 0x20760, v2
	ds_read2_b32 v[4:5], v4 offset1:1
	ds_read2_b32 v[6:7], v6 offset1:1
	v_add_u32_e32 v8, 0x206e8, v2
	v_add_u32_e32 v10, 0x20768, v2
	v_add_u32_e32 v12, 0x20700, v2
	v_add_u32_e32 v14, 0x20780, v2
	v_add_u32_e32 v16, 0x20708, v2
	v_add_u32_e32 v178, 0x20788, v2
	v_add_u32_e32 v180, 0x20720, v2
	v_add_u32_e32 v182, 0x207a0, v2
	v_add_u32_e32 v184, 0x20728, v2
	v_add_u32_e32 v186, 0x207a8, v2
	v_add_u32_e32 v188, 0x20740, v2
	v_add_u32_e32 v190, 0x207c0, v2
	v_add_u32_e32 v192, 0x20748, v2
	v_add_u32_e32 v2, 0x207c8, v2
	ds_read2_b32 v[8:9], v8 offset1:1
	ds_read2_b32 v[10:11], v10 offset1:1
	ds_read2_b32 v[12:13], v12 offset1:1
	ds_read2_b32 v[14:15], v14 offset1:1
	ds_read2_b32 v[16:17], v16 offset1:1
	ds_read2_b32 v[178:179], v178 offset1:1
	ds_read2_b32 v[180:181], v180 offset1:1
	ds_read2_b32 v[182:183], v182 offset1:1
	ds_read2_b32 v[184:185], v184 offset1:1
	ds_read2_b32 v[186:187], v186 offset1:1
	ds_read2_b32 v[188:189], v188 offset1:1
	ds_read2_b32 v[190:191], v190 offset1:1
	ds_read2_b32 v[192:193], v192 offset1:1
	s_waitcnt lgkmcnt(14)
	v_add_f32_e32 v162, v162, v4
	v_add_f32_e32 v163, v163, v5
	ds_read2_b32 v[4:5], v2 offset1:1
	s_waitcnt lgkmcnt(3)
	v_add_f32_e32 v174, v174, v188
	v_add_f32_e32 v175, v175, v189
	v_add_f32_e32 v172, v172, v184
	v_add_f32_e32 v173, v173, v185
	s_waitcnt lgkmcnt(1)
	v_add_f32_e32 v176, v176, v192
	v_add_f32_e32 v177, v177, v193
	v_add_f32_e32 v170, v170, v180
	v_add_f32_e32 v171, v171, v181
	v_add_f32_e32 v168, v168, v16
	v_add_f32_e32 v169, v169, v17
	v_add_f32_e32 v166, v166, v12
	v_add_f32_e32 v167, v167, v13
	v_add_f32_e32 v164, v164, v8
	v_add_f32_e32 v165, v165, v9
	s_waitcnt lgkmcnt(0)
	v_add_f32_e32 v160, v160, v4
	v_add_f32_e32 v161, v161, v5
	v_add_f32_e32 v158, v158, v190
	v_add_f32_e32 v159, v159, v191
	v_add_f32_e32 v156, v156, v186
	v_add_f32_e32 v157, v157, v187
	v_add_f32_e32 v154, v154, v182
	v_add_f32_e32 v155, v155, v183
	v_add_f32_e32 v152, v152, v178
	v_add_f32_e32 v153, v153, v179
	v_add_f32_e32 v150, v150, v14
	v_add_f32_e32 v151, v151, v15
	v_add_f32_e32 v148, v148, v10
	v_add_f32_e32 v149, v149, v11
	v_add_f32_e32 v146, v146, v6
	v_add_f32_e32 v147, v147, v7

.LBB0_457:
	s_and_b64 vcc, exec, s[10:11]
	s_cbranch_vccz .LBB0_423
	s_and_b64 vcc, exec, s[8:9]
	s_cbranch_vccnz .LBB0_422
	v_exp_f32_e64 v4, -v2
	s_nop 0
	v_mul_f32_e32 v144, v144, v4
	v_mul_f32_e32 v145, v145, v4
	v_mul_f32_e32 v142, v142, v4
	v_mul_f32_e32 v143, v143, v4
	v_mul_f32_e32 v140, v140, v4
	v_mul_f32_e32 v141, v141, v4
	v_mul_f32_e32 v138, v138, v4
	v_mul_f32_e32 v139, v139, v4
	v_mul_f32_e32 v136, v136, v4
	v_mul_f32_e32 v137, v137, v4
	v_mul_f32_e32 v134, v134, v4
	v_mul_f32_e32 v135, v135, v4
	v_mul_f32_e32 v132, v132, v4
	v_mul_f32_e32 v133, v133, v4
	v_mul_f32_e32 v130, v130, v4
	v_mul_f32_e32 v131, v131, v4
	v_mul_f32_e32 v112, v112, v4
	v_mul_f32_e32 v113, v113, v4
	v_mul_f32_e32 v110, v110, v4
	v_mul_f32_e32 v111, v111, v4
	v_mul_f32_e32 v108, v108, v4
	v_mul_f32_e32 v109, v109, v4
	v_mul_f32_e32 v106, v106, v4
	v_mul_f32_e32 v107, v107, v4
	v_mul_f32_e32 v104, v104, v4
	v_mul_f32_e32 v105, v105, v4
	v_mul_f32_e32 v102, v102, v4
	v_mul_f32_e32 v103, v103, v4
	v_mul_f32_e32 v100, v100, v4
	v_mul_f32_e32 v101, v101, v4
	v_mul_f32_e32 v98, v98, v4
	v_mul_f32_e32 v99, v99, v4
	v_mul_f32_e32 v80, v80, v4
	v_mul_f32_e32 v81, v81, v4
	v_mul_f32_e32 v78, v78, v4
	v_mul_f32_e32 v79, v79, v4
	v_mul_f32_e32 v76, v76, v4
	v_mul_f32_e32 v77, v77, v4
	v_mul_f32_e32 v74, v74, v4
	v_mul_f32_e32 v75, v75, v4
	v_mul_f32_e32 v72, v72, v4
	v_mul_f32_e32 v73, v73, v4
	v_mul_f32_e32 v70, v70, v4
	v_mul_f32_e32 v71, v71, v4
	v_mul_f32_e32 v68, v68, v4
	v_mul_f32_e32 v69, v69, v4
	v_mul_f32_e32 v66, v66, v4
	v_mul_f32_e32 v67, v67, v4
	v_mul_f32_e32 v48, v48, v4
	v_mul_f32_e32 v49, v49, v4
	v_mul_f32_e32 v46, v46, v4
	v_mul_f32_e32 v47, v47, v4
	v_mul_f32_e32 v44, v44, v4
	v_mul_f32_e32 v45, v45, v4
	v_mul_f32_e32 v42, v42, v4
	v_mul_f32_e32 v43, v43, v4
	v_mul_f32_e32 v40, v40, v4
	v_mul_f32_e32 v41, v41, v4
	v_mul_f32_e32 v38, v38, v4
	v_mul_f32_e32 v39, v39, v4
	v_mul_f32_e32 v36, v36, v4
	v_mul_f32_e32 v37, v37, v4
	v_mul_f32_e32 v34, v34, v4
	v_mul_f32_e32 v35, v35, v4
	v_mul_f32_e32 v215, v215, v4
	s_branch .LBB0_422
